# P1 plain projection tiles: weight rows permuted at the LDS-DMA source so a wave owns 64 contiguous columns; epilogue lane exchange + 128-byte-per-row stores
# baseline (speedup 1.0000x reference)
; #define PG8_WAIT_V(n) asm volatile("s_waitcnt vmcnt(" #n ")" ::: "memory")
; #define PG8_BAR __builtin_amdgcn_s_barrier()
; template <class Epi, class Sched, bool ALIGN_EPI = false, bool SP2 = false>
; __device__ __forceinline__ void gemm_phase(PG8_LAS unsigned char* lds, const Gemm g, const Sched& S, const Epi& E) {
;     ...
;     for (int i = 0; i < 2; ++i) { int R, C; stage_rc(tid * 16 + i * 8192, R, C); const int Rb = Epi::PERM ? ((R & ~31) + perm32(R & 31)) : R;
;         voffA[i] = (unsigned)(R * K + C) * 2u; voffB[i] = (unsigned)(Rb * K + C) * 2u; }
;     const size_t kstep = (size_t)(BK * 2);
;     const size_t hstep = (size_t)HALF * K * 2;
;     const size_t tstep = 2 * hstep;
;     const unsigned ldsw = (unsigned)wid * 1024u;
;     const int aoff = lds_byte(wr * 64 + fr, fq * 8), boff = lds_byte(wc * 32 + fr, fq * 8);
;     ...
;     Unit cur, nxt; int ui = 0;
;     if (!S.next(0, cur)) return;
;     f32x4 acc[2][2][4][2];
; #pragma unroll
;     for (int a = 0; a < 2; ++a)
; #pragma unroll
;         for (int b = 0; b < 2; ++b)
; #pragma unroll
;             for (int m = 0; m < 4; ++m)
; #pragma unroll
;                 for (int n = 0; n < 2; ++n) acc[a][b][m][n] = (f32x4){0.f, 0.f, 0.f, 0.f};
;     bf16x8 At[4][2], B0[2][2], B1[2][2];
;     const char* cA = (const char*)g.A + (size_t)cur.pm * tstep; const char* cB = (const char*)g.Bt + (size_t)cur.pn * tstep;
;     S.a_ready(cur);
;     if constexpr (SP2) {
;         PG8_STAGE(PG8_SB(0, 0), cB, voffB); PG8_STAGE(PG8_SB(0, 1), cB + hstep, voffB); PG8_STAGE(PG8_SA(0, 0), cA, voffA); PG8_STAGE(PG8_SA(0, 1), cA + hstep, voffA);
;         if (wr == 1) PG8_BAR;
;         PG8_WAIT_V(2); PG8_BAR;
;         PG8_STAGE(PG8_SB(1, 0), cB + kstep, voffB); PG8_STAGE(PG8_SA(1, 0), cA + kstep, voffA); PG8_STAGE(PG8_SB(1, 1), cB + hstep + kstep, voffB);
;         PG8_WAIT_V(6); PG8_BAR;
;     } else {
;         PG8_STAGE(PG8_SB(0, 0), cB, voffB); PG8_STAGE(PG8_SA(0, 0), cA, voffA); PG8_STAGE(PG8_SB(0, 1), cB + hstep, voffB); PG8_STAGE(PG8_SA(0, 1), cA + hstep, voffA);
;         if (wr == 1) PG8_BAR;
;         PG8_WAIT_V(4); PG8_BAR;
;         PG8_STAGE(PG8_SB(1, 0), cB + kstep, voffB); PG8_STAGE(PG8_SA(1, 0), cA + kstep, voffA); PG8_STAGE(PG8_SB(1, 1), cB + hstep + kstep, voffB);
;         PG8_WAIT_V(6); PG8_BAR;
.LBB0_144:
	v_readlane_b32 s0, v253, 41
	v_readlane_b32 s1, v253, 42
	s_lshl_b32 s16, s0, 6
	v_readlane_b32 s4, v252, 6
	v_readlane_b32 s0, v252, 53
	v_mov_b32_e32 v1, v0
	v_readlane_b32 s10, v252, 12
	v_readlane_b32 s11, v252, 13
	v_mov_b32_e32 v15, v0
	v_readlane_b32 s1, v252, 54
	s_mov_b32 s17, s3
	s_andn2_b64 vcc, exec, s[0:1]
	v_readfirstlane_b32 s1, v15
	v_readlane_b32 s5, v252, 7
	v_readlane_b32 s6, v252, 8
	v_readlane_b32 s7, v252, 9
	v_readlane_b32 s8, v252, 10
	v_readlane_b32 s9, v252, 11
	s_cbranch_vccnz .LBB0_222
	v_lshlrev_b32_e32 v1, 4, v15
	v_add_u32_e32 v2, 0x2000, v1
	v_ashrrev_i32_e32 v4, 31, v2
	v_lshrrev_b32_e32 v4, 22, v4
	v_add_u32_e32 v4, v2, v4
	v_ashrrev_i32_e32 v12, 10, v4
	v_mul_i32_i24_e32 v4, 0x400, v12
	v_sub_u32_e32 v2, v2, v4
	v_lshrrev_b32_e32 v4, 4, v2
	v_bitop3_b32 v2, v4, v2, 32 bitop3:0x6c
	v_ashrrev_i32_e32 v4, 31, v2
	v_lshrrev_b32_e32 v4, 26, v4
	v_add_u32_e32 v4, v2, v4
	s_waitcnt lgkmcnt(0)
	v_lshlrev_b32_e32 v5, 3, v12
	v_ashrrev_i32_e32 v13, 6, v4
	v_and_b32_e32 v5, -16, v5
	v_readlane_b32 s4, v253, 41
	v_add_u32_e32 v5, v13, v5
	s_mul_i32 s0, s4, 0xe800000
	v_and_b32_e32 v6, 3, v13
	s_mov_b32 s4, 0x7ffe0
	v_lshrrev_b32_e32 v7, 2, v5
	v_lshlrev_b32_e32 v8, 1, v5
	v_and_b32_e32 v4, 0xc0, v4
	v_and_or_b32 v6, v5, s4, v6
	v_and_b32_e32 v7, 4, v7
	v_and_b32_e32 v8, 24, v8
	v_sub_u32_e32 v2, v2, v4
	v_or3_b32 v6, v6, v7, v8
	v_lshlrev_b32_e32 v7, 5, v12
	v_ashrrev_i16_sdwa v2, v227, sext(v2) dst_sel:DWORD dst_unused:UNUSED_PAD src0_sel:DWORD src1_sel:BYTE_0
	v_and_b32_e32 v7, 32, v7
	v_bfe_i32 v14, v2, 0, 16
	v_add_lshl_u32 v2, v7, v14, 1
	v_lshl_add_u32 v132, v6, 13, v2
	v_lshl_add_u32 v134, v5, 13, v2
	v_bfe_i32 v2, v15, 27, 1
	v_lshrrev_b32_e32 v2, 22, v2
	v_add_u32_e32 v2, v1, v2
	v_and_b32_e32 v2, 0xfffffc00, v2
	v_sub_u32_e32 v1, v1, v2
	v_lshrrev_b32_e32 v2, 4, v1
	v_ashrrev_i32_e32 v4, 31, v15
	v_bitop3_b32 v1, v2, v1, 32 bitop3:0x6c
	v_lshrrev_b32_e32 v4, 26, v4
	v_ashrrev_i32_e32 v2, 31, v1
	v_add_u32_e32 v4, v15, v4
	s_add_u32 s54, s10, 0x27100000
	v_lshrrev_b32_e32 v2, 26, v2
	v_ashrrev_i32_e32 v17, 6, v4
	s_addc_u32 s55, s11, 0
	v_add_u32_e32 v2, v1, v2
	v_lshlrev_b32_e32 v4, 3, v17
	s_add_u32 s0, s10, s0
	v_ashrrev_i32_e32 v16, 6, v2
	v_and_b32_e32 v4, -16, v4
	s_addc_u32 s2, s11, 0
	v_add_u32_e32 v4, v16, v4
	s_add_u32 s56, s0, 0x100000
	v_and_b32_e32 v5, 3, v16
	v_lshrrev_b32_e32 v6, 2, v4
	v_lshlrev_b32_e32 v7, 1, v4
	v_and_b32_e32 v2, 0xc0, v2
	v_readlane_b32 s5, v253, 42
	s_addc_u32 s57, s2, 0
	s_ashr_i32 s2, s1, 6
	v_and_or_b32 v5, v4, s4, v5
	v_and_b32_e32 v6, 4, v6
	v_and_b32_e32 v7, 24, v7
	v_sub_u32_e32 v1, v1, v2
	s_ashr_i32 s0, s1, 8
	s_lshl_b32 s58, s2, 10
	v_or3_b32 v5, v5, v6, v7
	v_lshlrev_b32_e32 v6, 5, v17
	v_ashrrev_i16_sdwa v1, v227, sext(v1) dst_sel:DWORD dst_unused:UNUSED_PAD src0_sel:DWORD src1_sel:BYTE_0
	v_readlane_b32 s4, v253, 11
	v_and_b32_e32 v6, 32, v6
	v_bfe_i32 v18, v1, 0, 16
	v_readlane_b32 s5, v253, 12
	s_add_u32 s46, s56, s4
	v_add_lshl_u32 v1, v6, v18, 1
	s_addc_u32 s47, s57, s5
	s_add_i32 s59, s58, 0
	v_lshl_add_u32 v2, v5, 13, v1
	v_lshl_add_u32 v136, v4, 13, v1
	v_readlane_b32 s100, v253, 11
	s_nop 0
	s_lshr_b32 s100, s100, 23
	s_lshr_b32 s100, 0x855, s100
	s_bitcmp1_b32 s100, 0
	s_cselect_b32 s100, 0xc0000, 0
	s_mov_b32 s101, 0x100000
	s_cselect_b32 s101, 0x40000, s101
	v_and_b32_e32 v218, s100, v2
	v_add_u32_e32 v218, v218, v2
	v_and_b32_e32 v220, s100, v132
	v_add_u32_e32 v220, v220, v132
	v_add_u32_e32 v224, s101, v218
	v_add_u32_e32 v226, s101, v220
	s_add_i32 m0, s59, 0x10000
	s_add_u32 s100, s46, 0x80
	s_addc_u32 s101, s47, 0
	global_load_lds_dwordx4 v218, s[46:47]
	s_add_i32 m0, s59, 0x12000
	s_add_u32 s4, s46, 0x100000
	global_load_lds_dwordx4 v220, s[46:47]
	s_addc_u32 s5, s47, 0
	s_add_i32 m0, s59, 0x14000
	v_mov_b32_e32 v133, v3
	global_load_lds_dwordx4 v224, s[46:47]
	s_add_i32 m0, s59, 0x16000
	v_mov_b32_e32 v137, v3
	global_load_lds_dwordx4 v226, s[46:47]
	v_readlane_b32 s4, v253, 9
	v_readlane_b32 s5, v253, 10
	s_add_u32 s12, s54, s4
	s_addc_u32 s13, s55, s5
	s_add_i32 s60, s59, 0x2000
	s_mov_b32 m0, s59
	s_add_u32 s4, s12, 0x100000
	global_load_lds_dwordx4 v136, s[12:13]
	s_mov_b32 m0, s60
	s_addc_u32 s5, s13, 0
	s_add_i32 s61, s59, 0x4000
	global_load_lds_dwordx4 v134, s[12:13]
	s_mov_b32 m0, s61
	s_add_i32 s62, s59, 0x6000
	global_load_lds_dwordx4 v136, s[4:5]
	s_mov_b32 m0, s62
	v_mov_b32_e32 v135, v3
	global_load_lds_dwordx4 v134, s[4:5]
	s_cmp_eq_u32 s0, 1
	v_lshl_add_u64 v[10:11], s[46:47], 0, v[2:3]
	v_lshl_add_u64 v[8:9], s[46:47], 0, v[132:133]
	v_lshl_add_u64 v[4:5], s[12:13], 0, v[136:137]
	s_cselect_b64 s[18:19], -1, 0
	s_cmp_lg_u32 s0, 1
	v_lshl_add_u64 v[6:7], s[12:13], 0, v[134:135]
	s_cbranch_scc1 .LBB0_147
	s_barrier
; #define PG8_STAGE(bufoff, gbase, voff) do { _Pragma("unroll") for (int _i = 0; _i < 2; ++_i) \
;         __builtin_amdgcn_global_load_lds((const unsigned*)((const char*)(gbase) + (voff)[_i]), (PG8_LAS unsigned*)(lds + (bufoff) + ldsw + _i * 8192), 16, 0, 0); } while (0)
; #define PG8_WAIT_V(n) asm volatile("s_waitcnt vmcnt(" #n ")" ::: "memory")
; #define PG8_BAR __builtin_amdgcn_s_barrier()
; template <class Epi, class Sched, bool ALIGN_EPI = false, bool SP2 = false>
; __device__ __forceinline__ void gemm_phase(PG8_LAS unsigned char* lds, const Gemm g, const Sched& S, const Epi& E) {
;     ...
;     const int tid = tid_l, wid = __builtin_amdgcn_readfirstlane(tid >> 6), lane = tid & 63, wr = wid >> 2, wc = wid & 3, fr = lane & 15, fq = lane >> 4;
;     const int K = g.K, nt = K / BK;
;     unsigned voffA[2], voffB[2];
; #pragma unroll
;     for (int i = 0; i < 2; ++i) { int R, C; stage_rc(tid * 16 + i * 8192, R, C); const int Rb = Epi::PERM ? ((R & ~31) + perm32(R & 31)) : R;
;         voffA[i] = (unsigned)(R * K + C) * 2u; voffB[i] = (unsigned)(Rb * K + C) * 2u; }
;     const size_t kstep = (size_t)(BK * 2);
;     const size_t hstep = (size_t)HALF * K * 2;
;     const size_t tstep = 2 * hstep;
;     const unsigned ldsw = (unsigned)wid * 1024u;
;     const int aoff = lds_byte(wr * 64 + fr, fq * 8), boff = lds_byte(wc * 32 + fr, fq * 8);
;     ...
;         PG8_STAGE(PG8_SB(1, 0), cB + kstep, voffB); PG8_STAGE(PG8_SA(1, 0), cA + kstep, voffA); PG8_STAGE(PG8_SB(1, 1), cB + hstep + kstep, voffB);
;         PG8_WAIT_V(6); PG8_BAR;
.LBB0_147:
	v_readlane_b32 s4, v253, 34
	v_readlane_b32 s5, v253, 35
	s_and_b64 s[4:5], s[4:5], exec
	s_mov_b32 s4, 0x3b100000
	s_cselect_b32 s4, s4, 0x80000
	s_add_u32 s20, s10, 0x3c120000
	s_addc_u32 s21, s11, 0
	s_add_u32 s22, s10, s4
	s_addc_u32 s23, s11, 0
	s_add_u32 s63, s10, 0x63160000
	s_addc_u32 s64, s11, 0
	s_add_u32 s24, s10, 0x6f560000
	s_addc_u32 s25, s11, 0
	s_lshl_b64 s[4:5], s[16:17], 2
	s_add_u32 s4, s10, s4
	s_addc_u32 s5, s11, s5
	s_add_u32 s4, s4, 0x3400
	s_addc_u32 s5, s5, 0
	v_writelane_b32 v253, s4, 48
	s_and_b32 s28, s2, 3
	s_add_i32 m0, s59, 0x18000
	v_writelane_b32 v253, s5, 49
	v_lshl_add_u64 v[10:11], v[10:11], 0, s[78:79]
	v_readlane_b32 s4, v253, 41
	s_lshl_b32 s2, s0, 13
	s_lshl_b32 s30, s28, 5
	s_lshl_b32 s6, s28, 12
	s_add_i32 s65, s4, 1
	s_waitcnt vmcnt(2)
	s_barrier
	global_load_lds_dwordx4 v218, s[100:101]
	v_lshl_add_u64 v[8:9], v[8:9], 0, s[78:79]
	s_add_i32 m0, s59, 0x1a000
	s_add_i32 s66, s59, 0x8000
	s_add_i32 s67, s59, 0xa000
	v_readlane_b32 s5, v253, 42
	global_load_lds_dwordx4 v220, s[100:101]
	v_lshl_add_u64 v[4:5], v[4:5], 0, s[78:79]
	s_mov_b32 m0, s66
	s_add_u32 s4, s46, 0x100080
	global_load_lds_dwordx4 v[4:5], off
	v_lshl_add_u64 v[4:5], v[6:7], 0, s[78:79]
	s_mov_b32 m0, s67
	s_addc_u32 s5, s47, 0
	global_load_lds_dwordx4 v[4:5], off
	s_add_i32 m0, s59, 0x1c000
	v_lshl_add_u64 v[4:5], s[4:5], 0, v[2:3]
	global_load_lds_dwordx4 v224, s[100:101]
	v_lshl_add_u64 v[4:5], s[4:5], 0, v[132:133]
	s_add_i32 m0, s59, 0x1e000
	s_cmpk_lt_u32 s1, 0x100
	global_load_lds_dwordx4 v226, s[100:101]
	s_cselect_b64 s[34:35], -1, 0
	s_ashr_i32 s1, s0, 31
	v_bfe_u32 v5, v15, 4, 2
	s_lshl_b64 s[38:39], s[0:1], 9
	s_or_b32 s1, s28, s0
	v_and_b32_e32 v4, 15, v15
	v_lshlrev_b32_e32 v6, 4, v5
	v_lshlrev_b32_e32 v7, 2, v15
	s_cmp_eq_u32 s1, 0
	v_lshl_or_b32 v6, v4, 6, v6
	v_and_b32_e32 v7, 32, v7
	s_cselect_b64 s[36:37], -1, 0
	s_add_u32 s1, s10, s38
	v_bitop3_b32 v8, v6, s2, v7 bitop3:0xde
	s_addc_u32 s2, s11, s39
	s_lshl_b32 s27, s28, 7
	s_add_u32 s38, s1, s27
	v_lshl_or_b32 v1, s0, 6, v4
	s_waitcnt vmcnt(0)
	v_lshlrev_b32_e32 v138, 3, v5
	v_bitop3_b32 v190, v6, s6, v7 bitop3:0xde
	v_or_b32_e32 v6, v5, v4
	v_cmp_eq_u32_e64 s[6:7], 0, v4
	v_cmp_eq_u32_e64 s[8:9], 0, v5
	s_addc_u32 s39, s2, 0
	v_lshlrev_b32_e32 v4, 5, v5
	v_mov_b32_e32 v5, v3
	v_lshl_add_u64 v[4:5], s[38:39], 0, v[4:5]
	s_mov_b64 s[38:39], 0x59120000
	v_lshl_add_u64 v[140:141], v[4:5], 0, s[38:39]
	v_lshlrev_b32_e32 v4, 16, v17
	v_and_b32_e32 v4, 0xfffe0000, v4
	s_lshl_b32 s1, s28, 2
	v_lshl_add_u32 v4, v16, 13, v4
	v_and_b32_e32 v5, 1, v17
	s_add_u32 s1, s10, s1
	v_lshl_or_b32 v4, v5, 6, v4
	s_addc_u32 s2, s11, 0
	v_lshl_add_u32 v142, v18, 1, v4
	v_lshlrev_b32_e32 v4, 16, v12
	s_add_u32 s1, s1, 0x6f660000
	v_and_b32_e32 v4, 0xfffe0000, v4
	s_waitcnt vmcnt(6)
	v_writelane_b32 v253, s1, 50
	v_lshl_add_u32 v4, v13, 13, v4
	v_and_b32_e32 v5, 1, v12
	v_lshl_or_b32 v4, v5, 6, v4
	v_readlane_b32 s10, v253, 7
	s_mov_b32 s26, 0
	v_cmp_eq_u32_e64 s[4:5], 0, v6
	s_mov_b32 s29, s3
	s_mov_b32 s31, s3
	v_mov_b32_e32 v139, v3
	s_addc_u32 s27, s2, 0
	v_or_b32_e32 v191, s30, v138
	v_mov_b32_e32 v143, v3
	v_lshl_add_u32 v144, v14, 1, v4
	v_mov_b32_e32 v145, v3
	v_add_u32_e32 v196, 0, v8
	v_mov_b32_e32 v192, s65
	v_readlane_b32 s1, v252, 63
	s_mov_b32 s2, s10
	s_barrier
	v_readlane_b32 s11, v253, 8
	s_branch .LBB0_150

; #define PG8_STAGE(bufoff, gbase, voff) do { _Pragma("unroll") for (int _i = 0; _i < 2; ++_i) \
;         __builtin_amdgcn_global_load_lds((const unsigned*)((const char*)(gbase) + (voff)[_i]), (PG8_LAS unsigned*)(lds + (bufoff) + ldsw + _i * 8192), 16, 0, 0); } while (0)
; #define PG8_LDA(dst, b, h) do { _Pragma("unroll") for (int m = 0; m < 4; ++m) _Pragma("unroll") for (int k = 0; k < 2; ++k) dst[m][k] = *(const PG8_LAS bf16x8*)(lds + PG8_SA(b, h) + aoff + m * 2048 + k * 1024); } while (0)
; #define PG8_LDB(dst, b, h) do { _Pragma("unroll") for (int n = 0; n < 2; ++n) _Pragma("unroll") for (int k = 0; k < 2; ++k) dst[n][k] = *(const PG8_LAS bf16x8*)(lds + PG8_SB(b, h) + boff + n * 2048 + k * 1024); } while (0)
; #define PG8_MMA(ai, bj, At, Bt) do { __builtin_amdgcn_s_setprio(1); _Pragma("unroll") for (int m = 0; m < 4; ++m) _Pragma("unroll") for (int n = 0; n < 2; ++n) _Pragma("unroll") for (int k = 0; k < 2; ++k) \
;         acc[ai][bj][m][n] = __builtin_amdgcn_mfma_f32_16x16x32_bf16(Bt[n][k], At[m][k], acc[ai][bj][m][n], 0, 0, 0); __builtin_amdgcn_s_setprio(0); } while (0)
; #define PG8_BAR __builtin_amdgcn_s_barrier()
; template <class Epi, class Sched, bool ALIGN_EPI = false, bool SP2 = false>
; __device__ __forceinline__ void gemm_phase(PG8_LAS unsigned char* lds, const Gemm g, const Sched& S, const Epi& E) {
;     ...
;             const bool last = (t == nt - 2);
;             const char* a1 = cA + (size_t)(t + 1) * kstep;
;             const char* a2 = last ? nA : cA + (size_t)(t + 2) * kstep; const char* b2 = last ? nB : cB + (size_t)(t + 2) * kstep;
;             const char* a3 = a2 + kstep; const char* b3 = b2 + kstep;
;             if (last && has_next) S.a_ready(nxt);
;             if constexpr (Epi::HAS_MID) { if (t != 0 && (t & (Epi::MID_EVERY - 1)) == 0) E.mid(acc, cur, t / Epi::MID_EVERY, wr, wc, fr, fq); }
;             if constexpr (SP2) {
;             PG8_LDB(B0, 0, 0); PG8_LDB(B1, 0, 1); PG8_SCHED; PG8_LDA(At, 0, 0); PG8_STAGE(PG8_SA(1, 1), a1 + hstep, voffA);
;             PG8_WAIT_V(8); PG8_WAIT_L(0); PG8_BAR; PG8_MMA(0, 0, At, B0); PG8_MMA(0, 1, At, B1); PG8_BAR; PG8_SCHED;
;             PG8_LDA(At, 0, 1); PG8_STAGE(PG8_SB(0, 0), b2, voffB); PG8_STAGE(PG8_SB(0, 1), b2 + hstep, voffB); PG8_STAGE(PG8_SA(0, 0), a2, voffA);
;             PG8_WAIT_V(8); PG8_WAIT_L(0); PG8_BAR; PG8_MMA(1, 0, At, B0); PG8_MMA(1, 1, At, B1); PG8_BAR; PG8_SCHED;
.LBB0_153:
	s_add_u32 s46, s12, 0xfff00080
	s_addc_u32 s47, s13, -1
	s_add_i32 s81, 0, 0x10000
	s_cmp_eq_u32 s80, 60
	s_cselect_b32 s49, s41, s47
	s_cselect_b32 s48, s50, s46
	s_cselect_b32 s47, s39, s53
	s_cselect_b32 s46, s51, s52
	s_cbranch_scc0 .Lp1_bmode_keep
	s_lshr_b32 s100, s38, 2
	s_lshr_b32 s100, 0x855, s100
	s_bitcmp1_b32 s100, 0
	s_cselect_b32 s100, 0xc0000, 0
	s_mov_b32 s101, 0x100000
	s_cselect_b32 s101, 0x40000, s101
	v_and_b32_e32 v218, s100, v2
	v_add_u32_e32 v218, v218, v2
	v_and_b32_e32 v220, s100, v132
	v_add_u32_e32 v220, v220, v132
	v_add_u32_e32 v224, s101, v218
	v_add_u32_e32 v226, s101, v220
.Lp1_bmode_keep:
	s_add_i32 s84, 0, 0x14000
	v_add_u32_e32 v158, s81, v190
	v_add_u32_e32 v174, s84, v190
	s_waitcnt lgkmcnt(0)
	ds_read_b128 v[146:149], v158
	ds_read_b128 v[150:153], v158 offset:1024
	ds_read_b128 v[154:157], v158 offset:2048
	ds_read_b128 v[158:161], v158 offset:3072
	ds_read_b128 v[162:165], v174
	ds_read_b128 v[166:169], v174 offset:1024
	ds_read_b128 v[170:173], v174 offset:2048
	ds_read_b128 v[174:177], v174 offset:3072
	v_lshl_add_u64 v[194:195], s[12:13], 0, v[142:143]
	s_add_i32 m0, s59, 0xc000
	ds_read_b128 v[178:181], v196
	ds_read_b128 v[182:185], v196 offset:1024
	ds_read_b128 v[186:189], v196 offset:2048
	ds_read_b128 v[198:201], v196 offset:3072
	ds_read_b128 v[202:205], v196 offset:4096
	ds_read_b128 v[206:209], v196 offset:5120
	ds_read_b128 v[210:213], v196 offset:6144
	ds_read_b128 v[214:217], v196 offset:7168
	global_load_lds_dwordx4 v[194:195], off
	v_lshl_add_u64 v[194:195], s[12:13], 0, v[144:145]
	s_add_i32 m0, s59, 0xe000
	s_nop 0
	global_load_lds_dwordx4 v[194:195], off
	s_waitcnt vmcnt(8)
	s_waitcnt lgkmcnt(0)
	s_barrier
	s_setprio 1
	s_waitcnt lgkmcnt(0)
	v_mfma_f32_16x16x32_bf16 v[128:131], v[146:149], v[178:181], v[128:131]
	v_mfma_f32_16x16x32_bf16 v[124:127], v[154:157], v[178:181], v[124:127]
	v_mfma_f32_16x16x32_bf16 v[112:115], v[146:149], v[186:189], v[112:115]
	v_mfma_f32_16x16x32_bf16 v[108:111], v[154:157], v[186:189], v[108:111]
	v_mfma_f32_16x16x32_bf16 v[96:99], v[146:149], v[202:205], v[96:99]
	v_mfma_f32_16x16x32_bf16 v[92:95], v[154:157], v[202:205], v[92:95]
	v_mfma_f32_16x16x32_bf16 v[80:83], v[146:149], v[210:213], v[80:83]
	v_mfma_f32_16x16x32_bf16 v[76:79], v[154:157], v[210:213], v[76:79]
	v_mfma_f32_16x16x32_bf16 v[128:131], v[150:153], v[182:185], v[128:131]
	v_mfma_f32_16x16x32_bf16 v[124:127], v[158:161], v[182:185], v[124:127]
	v_mfma_f32_16x16x32_bf16 v[112:115], v[150:153], v[198:201], v[112:115]
	v_mfma_f32_16x16x32_bf16 v[108:111], v[158:161], v[198:201], v[108:111]
	v_mfma_f32_16x16x32_bf16 v[96:99], v[150:153], v[206:209], v[96:99]
	v_mfma_f32_16x16x32_bf16 v[92:95], v[158:161], v[206:209], v[92:95]
	v_mfma_f32_16x16x32_bf16 v[80:83], v[150:153], v[214:217], v[80:83]
	v_mfma_f32_16x16x32_bf16 v[76:79], v[158:161], v[214:217], v[76:79]
	s_setprio 0
	s_setprio 1
	v_mfma_f32_16x16x32_bf16 v[120:123], v[162:165], v[178:181], v[120:123]
	v_mfma_f32_16x16x32_bf16 v[116:119], v[170:173], v[178:181], v[116:119]
	v_mfma_f32_16x16x32_bf16 v[104:107], v[162:165], v[186:189], v[104:107]
	v_mfma_f32_16x16x32_bf16 v[100:103], v[170:173], v[186:189], v[100:103]
	v_mfma_f32_16x16x32_bf16 v[88:91], v[162:165], v[202:205], v[88:91]
	v_mfma_f32_16x16x32_bf16 v[84:87], v[170:173], v[202:205], v[84:87]
	v_mfma_f32_16x16x32_bf16 v[72:75], v[162:165], v[210:213], v[72:75]
	v_mfma_f32_16x16x32_bf16 v[68:71], v[170:173], v[210:213], v[68:71]
	v_mfma_f32_16x16x32_bf16 v[120:123], v[166:169], v[182:185], v[120:123]
	v_mfma_f32_16x16x32_bf16 v[116:119], v[174:177], v[182:185], v[116:119]
	v_mfma_f32_16x16x32_bf16 v[104:107], v[166:169], v[198:201], v[104:107]
	v_mfma_f32_16x16x32_bf16 v[100:103], v[174:177], v[198:201], v[100:103]
	v_mfma_f32_16x16x32_bf16 v[88:91], v[166:169], v[206:209], v[88:91]
	v_mfma_f32_16x16x32_bf16 v[84:87], v[174:177], v[206:209], v[84:87]
	v_mfma_f32_16x16x32_bf16 v[72:75], v[166:169], v[214:217], v[72:75]
	v_mfma_f32_16x16x32_bf16 v[68:71], v[174:177], v[214:217], v[68:71]
	s_setprio 0
	s_barrier
	s_add_i32 s81, s81, s58
	s_mov_b32 m0, s81
	ds_read_b128 v[178:181], v196 offset:16384
	ds_read_b128 v[182:185], v196 offset:17408
	ds_read_b128 v[186:189], v196 offset:18432
	ds_read_b128 v[198:201], v196 offset:19456
	ds_read_b128 v[202:205], v196 offset:20480
	ds_read_b128 v[206:209], v196 offset:21504
	ds_read_b128 v[210:213], v196 offset:22528
	ds_read_b128 v[214:217], v196 offset:23552
	global_load_lds_dwordx4 v218, s[46:47]
	s_add_i32 m0, s81, 0x2000
	s_add_i32 s81, s84, s58
	s_nop 0
	global_load_lds_dwordx4 v220, s[46:47]
	s_mov_b32 m0, s81
	v_lshl_add_u64 v[234:235], s[48:49], 0, v[134:135]
	global_load_lds_dwordx4 v224, s[46:47]
	s_add_i32 m0, s81, 0x2000
	s_nop 0
	global_load_lds_dwordx4 v226, s[46:47]
	v_lshl_add_u64 v[232:233], s[48:49], 0, v[136:137]
	s_mov_b32 m0, s59
	s_nop 0
	global_load_lds_dwordx4 v[232:233], off
	s_mov_b32 m0, s60
	s_nop 0
	global_load_lds_dwordx4 v[234:235], off
	s_waitcnt vmcnt(8)
	s_waitcnt lgkmcnt(0)
	s_barrier
; #define PG8_STAGE(bufoff, gbase, voff) do { _Pragma("unroll") for (int _i = 0; _i < 2; ++_i) \
;         __builtin_amdgcn_global_load_lds((const unsigned*)((const char*)(gbase) + (voff)[_i]), (PG8_LAS unsigned*)(lds + (bufoff) + ldsw + _i * 8192), 16, 0, 0); } while (0)
; #define PG8_LDA(dst, b, h) do { _Pragma("unroll") for (int m = 0; m < 4; ++m) _Pragma("unroll") for (int k = 0; k < 2; ++k) dst[m][k] = *(const PG8_LAS bf16x8*)(lds + PG8_SA(b, h) + aoff + m * 2048 + k * 1024); } while (0)
; #define PG8_LDB(dst, b, h) do { _Pragma("unroll") for (int n = 0; n < 2; ++n) _Pragma("unroll") for (int k = 0; k < 2; ++k) dst[n][k] = *(const PG8_LAS bf16x8*)(lds + PG8_SB(b, h) + boff + n * 2048 + k * 1024); } while (0)
; #define PG8_MMA(ai, bj, At, Bt) do { __builtin_amdgcn_s_setprio(1); _Pragma("unroll") for (int m = 0; m < 4; ++m) _Pragma("unroll") for (int n = 0; n < 2; ++n) _Pragma("unroll") for (int k = 0; k < 2; ++k) \
;         acc[ai][bj][m][n] = __builtin_amdgcn_mfma_f32_16x16x32_bf16(Bt[n][k], At[m][k], acc[ai][bj][m][n], 0, 0, 0); __builtin_amdgcn_s_setprio(0); } while (0)
; #define PG8_WAIT_V(n) asm volatile("s_waitcnt vmcnt(" #n ")" ::: "memory")
; #define PG8_WAIT_L(n) asm volatile("s_waitcnt lgkmcnt(" #n ")" ::: "memory")
; #define PG8_BAR __builtin_amdgcn_s_barrier()
; #define PG8_SCHED __builtin_amdgcn_sched_barrier(0)
; template <class Epi, class Sched, bool ALIGN_EPI = false, bool SP2 = false>
; __device__ __forceinline__ void gemm_phase(PG8_LAS unsigned char* lds, const Gemm g, const Sched& S, const Epi& E) {
;     ...
;             PG8_WAIT_V(8); PG8_WAIT_L(0); PG8_BAR; PG8_MMA(0, 0, At, B0); PG8_MMA(0, 1, At, B1); PG8_BAR; PG8_SCHED;
;             PG8_LDA(At, 0, 1); PG8_STAGE(PG8_SB(0, 0), b2, voffB); PG8_STAGE(PG8_SB(0, 1), b2 + hstep, voffB); PG8_STAGE(PG8_SA(0, 0), a2, voffA);
;             PG8_WAIT_V(8); PG8_WAIT_L(0); PG8_BAR; PG8_MMA(1, 0, At, B0); PG8_MMA(1, 1, At, B1); PG8_BAR; PG8_SCHED;
;             PG8_LDB(B0, 1, 0); PG8_LDB(B1, 1, 1); PG8_SCHED; PG8_LDA(At, 1, 0); PG8_STAGE(PG8_SA(0, 1), a2 + hstep, voffA);
;             PG8_WAIT_V(8); PG8_WAIT_L(0); PG8_BAR; PG8_MMA(0, 0, At, B0); PG8_MMA(0, 1, At, B1); PG8_BAR; PG8_SCHED;
	s_setprio 1
	s_waitcnt lgkmcnt(0)
	v_mfma_f32_16x16x32_bf16 v[64:67], v[146:149], v[178:181], v[64:67]
	v_mfma_f32_16x16x32_bf16 v[60:63], v[154:157], v[178:181], v[60:63]
	v_mfma_f32_16x16x32_bf16 v[48:51], v[146:149], v[186:189], v[48:51]
	v_mfma_f32_16x16x32_bf16 v[44:47], v[154:157], v[186:189], v[44:47]
	v_mfma_f32_16x16x32_bf16 v[32:35], v[146:149], v[202:205], v[32:35]
	v_mfma_f32_16x16x32_bf16 v[28:31], v[154:157], v[202:205], v[28:31]
	v_mfma_f32_16x16x32_bf16 v[16:19], v[146:149], v[210:213], v[16:19]
	v_mfma_f32_16x16x32_bf16 v[12:15], v[154:157], v[210:213], v[12:15]
	v_mfma_f32_16x16x32_bf16 v[64:67], v[150:153], v[182:185], v[64:67]
	v_mfma_f32_16x16x32_bf16 v[60:63], v[158:161], v[182:185], v[60:63]
	v_mfma_f32_16x16x32_bf16 v[48:51], v[150:153], v[198:201], v[48:51]
	v_mfma_f32_16x16x32_bf16 v[44:47], v[158:161], v[198:201], v[44:47]
	v_mfma_f32_16x16x32_bf16 v[32:35], v[150:153], v[206:209], v[32:35]
	v_mfma_f32_16x16x32_bf16 v[28:31], v[158:161], v[206:209], v[28:31]
	v_mfma_f32_16x16x32_bf16 v[16:19], v[150:153], v[214:217], v[16:19]
	v_mfma_f32_16x16x32_bf16 v[12:15], v[158:161], v[214:217], v[12:15]
	s_setprio 0
	s_setprio 1
	v_mfma_f32_16x16x32_bf16 v[56:59], v[162:165], v[178:181], v[56:59]
	v_mfma_f32_16x16x32_bf16 v[52:55], v[170:173], v[178:181], v[52:55]
	v_mfma_f32_16x16x32_bf16 v[40:43], v[162:165], v[186:189], v[40:43]
	v_mfma_f32_16x16x32_bf16 v[36:39], v[170:173], v[186:189], v[36:39]
	v_mfma_f32_16x16x32_bf16 v[24:27], v[162:165], v[202:205], v[24:27]
	v_mfma_f32_16x16x32_bf16 v[20:23], v[170:173], v[202:205], v[20:23]
	v_mfma_f32_16x16x32_bf16 v[8:11], v[162:165], v[210:213], v[8:11]
	v_mfma_f32_16x16x32_bf16 v[4:7], v[170:173], v[210:213], v[4:7]
	v_mfma_f32_16x16x32_bf16 v[56:59], v[166:169], v[182:185], v[56:59]
	v_mfma_f32_16x16x32_bf16 v[52:55], v[174:177], v[182:185], v[52:55]
	v_mfma_f32_16x16x32_bf16 v[40:43], v[166:169], v[198:201], v[40:43]
	v_mfma_f32_16x16x32_bf16 v[36:39], v[174:177], v[198:201], v[36:39]
	v_mfma_f32_16x16x32_bf16 v[24:27], v[166:169], v[206:209], v[24:27]
	v_mfma_f32_16x16x32_bf16 v[20:23], v[174:177], v[206:209], v[20:23]
	v_mfma_f32_16x16x32_bf16 v[8:11], v[166:169], v[214:217], v[8:11]
	v_mfma_f32_16x16x32_bf16 v[4:7], v[174:177], v[214:217], v[4:7]
	s_setprio 0
	s_barrier
	s_add_i32 s81, 0, 0x18000
	s_add_i32 s82, 0, 0x1c000
	v_add_u32_e32 v158, s81, v190
	v_add_u32_e32 v174, s82, v190
	ds_read_b128 v[146:149], v158
	ds_read_b128 v[150:153], v158 offset:1024
	ds_read_b128 v[154:157], v158 offset:2048
	ds_read_b128 v[158:161], v158 offset:3072
	ds_read_b128 v[162:165], v174
	ds_read_b128 v[166:169], v174 offset:1024
	ds_read_b128 v[170:173], v174 offset:2048
	ds_read_b128 v[174:177], v174 offset:3072
	s_add_u32 s48, s48, 0x100000
	s_addc_u32 s49, s49, 0
	s_mov_b32 m0, s61
	v_lshl_add_u64 v[236:237], s[48:49], 0, v[136:137]
	ds_read_b128 v[178:181], v196 offset:32768
	ds_read_b128 v[182:185], v196 offset:33792
	ds_read_b128 v[186:189], v196 offset:34816
	ds_read_b128 v[198:201], v196 offset:35840
	ds_read_b128 v[202:205], v196 offset:36864
	ds_read_b128 v[206:209], v196 offset:37888
	ds_read_b128 v[210:213], v196 offset:38912
	ds_read_b128 v[214:217], v196 offset:39936
	global_load_lds_dwordx4 v[236:237], off
	v_lshl_add_u64 v[236:237], s[48:49], 0, v[134:135]
	s_mov_b32 m0, s62
	s_nop 0
	global_load_lds_dwordx4 v[236:237], off
	s_waitcnt vmcnt(8)
	s_waitcnt lgkmcnt(0)
	s_barrier
	s_setprio 1
	s_waitcnt lgkmcnt(0)
	v_mfma_f32_16x16x32_bf16 v[128:131], v[146:149], v[178:181], v[128:131]
	v_mfma_f32_16x16x32_bf16 v[124:127], v[154:157], v[178:181], v[124:127]
	v_mfma_f32_16x16x32_bf16 v[112:115], v[146:149], v[186:189], v[112:115]
	v_mfma_f32_16x16x32_bf16 v[108:111], v[154:157], v[186:189], v[108:111]
	v_mfma_f32_16x16x32_bf16 v[96:99], v[146:149], v[202:205], v[96:99]
	v_mfma_f32_16x16x32_bf16 v[92:95], v[154:157], v[202:205], v[92:95]
	v_mfma_f32_16x16x32_bf16 v[80:83], v[146:149], v[210:213], v[80:83]
	v_mfma_f32_16x16x32_bf16 v[76:79], v[154:157], v[210:213], v[76:79]
	v_mfma_f32_16x16x32_bf16 v[128:131], v[150:153], v[182:185], v[128:131]
	v_mfma_f32_16x16x32_bf16 v[124:127], v[158:161], v[182:185], v[124:127]
	v_mfma_f32_16x16x32_bf16 v[112:115], v[150:153], v[198:201], v[112:115]
	v_mfma_f32_16x16x32_bf16 v[108:111], v[158:161], v[198:201], v[108:111]
	v_mfma_f32_16x16x32_bf16 v[96:99], v[150:153], v[206:209], v[96:99]
	v_mfma_f32_16x16x32_bf16 v[92:95], v[158:161], v[206:209], v[92:95]
	v_mfma_f32_16x16x32_bf16 v[80:83], v[150:153], v[214:217], v[80:83]
	v_mfma_f32_16x16x32_bf16 v[76:79], v[158:161], v[214:217], v[76:79]
	s_setprio 0
	s_setprio 1
	v_mfma_f32_16x16x32_bf16 v[120:123], v[162:165], v[178:181], v[120:123]
	v_mfma_f32_16x16x32_bf16 v[116:119], v[170:173], v[178:181], v[116:119]
	v_mfma_f32_16x16x32_bf16 v[104:107], v[162:165], v[186:189], v[104:107]
	v_mfma_f32_16x16x32_bf16 v[100:103], v[170:173], v[186:189], v[100:103]
	v_mfma_f32_16x16x32_bf16 v[88:91], v[162:165], v[202:205], v[88:91]
	v_mfma_f32_16x16x32_bf16 v[84:87], v[170:173], v[202:205], v[84:87]
	v_mfma_f32_16x16x32_bf16 v[72:75], v[162:165], v[210:213], v[72:75]
	v_mfma_f32_16x16x32_bf16 v[68:71], v[170:173], v[210:213], v[68:71]
	v_mfma_f32_16x16x32_bf16 v[120:123], v[166:169], v[182:185], v[120:123]
	v_mfma_f32_16x16x32_bf16 v[116:119], v[174:177], v[182:185], v[116:119]
	v_mfma_f32_16x16x32_bf16 v[104:107], v[166:169], v[198:201], v[104:107]
	v_mfma_f32_16x16x32_bf16 v[100:103], v[174:177], v[198:201], v[100:103]
	v_mfma_f32_16x16x32_bf16 v[88:91], v[166:169], v[206:209], v[88:91]
	v_mfma_f32_16x16x32_bf16 v[84:87], v[174:177], v[206:209], v[84:87]
	v_mfma_f32_16x16x32_bf16 v[72:75], v[166:169], v[214:217], v[72:75]
	v_mfma_f32_16x16x32_bf16 v[68:71], v[174:177], v[214:217], v[68:71]
	s_setprio 0
	s_barrier
; #define PG8_STAGE(bufoff, gbase, voff) do { _Pragma("unroll") for (int _i = 0; _i < 2; ++_i) \
;         __builtin_amdgcn_global_load_lds((const unsigned*)((const char*)(gbase) + (voff)[_i]), (PG8_LAS unsigned*)(lds + (bufoff) + ldsw + _i * 8192), 16, 0, 0); } while (0)
; #define PG8_LDA(dst, b, h) do { _Pragma("unroll") for (int m = 0; m < 4; ++m) _Pragma("unroll") for (int k = 0; k < 2; ++k) dst[m][k] = *(const PG8_LAS bf16x8*)(lds + PG8_SA(b, h) + aoff + m * 2048 + k * 1024); } while (0)
; #define PG8_MMA(ai, bj, At, Bt) do { __builtin_amdgcn_s_setprio(1); _Pragma("unroll") for (int m = 0; m < 4; ++m) _Pragma("unroll") for (int n = 0; n < 2; ++n) _Pragma("unroll") for (int k = 0; k < 2; ++k) \
;         acc[ai][bj][m][n] = __builtin_amdgcn_mfma_f32_16x16x32_bf16(Bt[n][k], At[m][k], acc[ai][bj][m][n], 0, 0, 0); __builtin_amdgcn_s_setprio(0); } while (0)
; #define PG8_WAIT_V(n) asm volatile("s_waitcnt vmcnt(" #n ")" ::: "memory")
; #define PG8_WAIT_L(n) asm volatile("s_waitcnt lgkmcnt(" #n ")" ::: "memory")
; #define PG8_BAR __builtin_amdgcn_s_barrier()
; #define PG8_SCHED __builtin_amdgcn_sched_barrier(0)
; template <class Epi, class Sched, bool ALIGN_EPI = false, bool SP2 = false>
; __device__ __forceinline__ void gemm_phase(PG8_LAS unsigned char* lds, const Gemm g, const Sched& S, const Epi& E) {
;     ...
;         for (int t = 0; t < nt; t += 2) {
;             const bool last = (t == nt - 2);
;             const char* a1 = cA + (size_t)(t + 1) * kstep;
;             const char* a2 = last ? nA : cA + (size_t)(t + 2) * kstep; const char* b2 = last ? nB : cB + (size_t)(t + 2) * kstep;
;             const char* a3 = a2 + kstep; const char* b3 = b2 + kstep;
;             if (last && has_next) S.a_ready(nxt);
;             if constexpr (Epi::HAS_MID) { if (t != 0 && (t & (Epi::MID_EVERY - 1)) == 0) E.mid(acc, cur, t / Epi::MID_EVERY, wr, wc, fr, fq); }
;     ...
;             PG8_LDA(At, 1, 1); PG8_STAGE(PG8_SB(1, 0), b3, voffB); PG8_STAGE(PG8_SB(1, 1), b3 + hstep, voffB); PG8_STAGE(PG8_SA(1, 0), a3, voffA);
;             PG8_WAIT_V(8); PG8_WAIT_L(0); PG8_BAR; PG8_MMA(1, 0, At, B0); PG8_MMA(1, 1, At, B1); PG8_BAR; PG8_SCHED;
	s_add_i32 s48, s81, s58
	s_add_u32 s100, s46, 0x80
	s_addc_u32 s101, s47, 0
	s_mov_b32 m0, s48
	ds_read_b128 v[178:181], v196 offset:49152
	ds_read_b128 v[182:185], v196 offset:50176
	ds_read_b128 v[186:189], v196 offset:51200
	ds_read_b128 v[198:201], v196 offset:52224
	ds_read_b128 v[202:205], v196 offset:53248
	ds_read_b128 v[206:209], v196 offset:54272
	ds_read_b128 v[210:213], v196 offset:55296
	ds_read_b128 v[214:217], v196 offset:56320
	global_load_lds_dwordx4 v218, s[100:101]
	s_add_i32 m0, s48, 0x2000
	s_add_i32 s48, s82, s58
	s_nop 0
	global_load_lds_dwordx4 v220, s[100:101]
	s_mov_b32 m0, s48
	s_nop 0
	global_load_lds_dwordx4 v224, s[100:101]
	s_add_i32 m0, s48, 0x2000
	s_nop 0
	global_load_lds_dwordx4 v226, s[100:101]
	v_lshl_add_u64 v[194:195], v[232:233], 0, s[78:79]
	s_mov_b32 m0, s66
	s_nop 0
	global_load_lds_dwordx4 v[194:195], off
	v_lshl_add_u64 v[194:195], v[234:235], 0, s[78:79]
	s_mov_b32 m0, s67
	s_nop 0
	global_load_lds_dwordx4 v[194:195], off
	s_waitcnt vmcnt(8)
	s_waitcnt lgkmcnt(0)
	s_barrier
	s_setprio 1
	s_waitcnt lgkmcnt(0)
	v_mfma_f32_16x16x32_bf16 v[64:67], v[146:149], v[178:181], v[64:67]
	v_mfma_f32_16x16x32_bf16 v[60:63], v[154:157], v[178:181], v[60:63]
	v_mfma_f32_16x16x32_bf16 v[48:51], v[146:149], v[186:189], v[48:51]
	v_mfma_f32_16x16x32_bf16 v[44:47], v[154:157], v[186:189], v[44:47]
	v_mfma_f32_16x16x32_bf16 v[32:35], v[146:149], v[202:205], v[32:35]
	v_mfma_f32_16x16x32_bf16 v[28:31], v[154:157], v[202:205], v[28:31]
	v_mfma_f32_16x16x32_bf16 v[16:19], v[146:149], v[210:213], v[16:19]
	v_mfma_f32_16x16x32_bf16 v[12:15], v[154:157], v[210:213], v[12:15]
	v_mfma_f32_16x16x32_bf16 v[64:67], v[150:153], v[182:185], v[64:67]
	v_mfma_f32_16x16x32_bf16 v[60:63], v[158:161], v[182:185], v[60:63]
	v_mfma_f32_16x16x32_bf16 v[48:51], v[150:153], v[198:201], v[48:51]
	v_mfma_f32_16x16x32_bf16 v[44:47], v[158:161], v[198:201], v[44:47]
	v_mfma_f32_16x16x32_bf16 v[32:35], v[150:153], v[206:209], v[32:35]
	v_mfma_f32_16x16x32_bf16 v[28:31], v[158:161], v[206:209], v[28:31]
	v_mfma_f32_16x16x32_bf16 v[16:19], v[150:153], v[214:217], v[16:19]
	v_mfma_f32_16x16x32_bf16 v[12:15], v[158:161], v[214:217], v[12:15]
	s_setprio 0
	s_setprio 1
	v_mfma_f32_16x16x32_bf16 v[56:59], v[162:165], v[178:181], v[56:59]
	v_mfma_f32_16x16x32_bf16 v[52:55], v[170:173], v[178:181], v[52:55]
	v_mfma_f32_16x16x32_bf16 v[40:43], v[162:165], v[186:189], v[40:43]
	v_mfma_f32_16x16x32_bf16 v[36:39], v[170:173], v[186:189], v[36:39]
	v_mfma_f32_16x16x32_bf16 v[24:27], v[162:165], v[202:205], v[24:27]
	v_mfma_f32_16x16x32_bf16 v[20:23], v[170:173], v[202:205], v[20:23]
	v_mfma_f32_16x16x32_bf16 v[8:11], v[162:165], v[210:213], v[8:11]
	v_mfma_f32_16x16x32_bf16 v[4:7], v[170:173], v[210:213], v[4:7]
	v_mfma_f32_16x16x32_bf16 v[56:59], v[166:169], v[182:185], v[56:59]
	v_mfma_f32_16x16x32_bf16 v[52:55], v[174:177], v[182:185], v[52:55]
	v_mfma_f32_16x16x32_bf16 v[40:43], v[166:169], v[198:201], v[40:43]
	v_mfma_f32_16x16x32_bf16 v[36:39], v[174:177], v[198:201], v[36:39]
	v_mfma_f32_16x16x32_bf16 v[24:27], v[166:169], v[206:209], v[24:27]
	v_mfma_f32_16x16x32_bf16 v[20:23], v[174:177], v[206:209], v[20:23]
	v_mfma_f32_16x16x32_bf16 v[8:11], v[166:169], v[214:217], v[8:11]
	v_mfma_f32_16x16x32_bf16 v[4:7], v[174:177], v[214:217], v[4:7]
	s_setprio 0
	s_barrier
	s_add_i32 s80, s80, 2
	s_add_u32 s12, s12, 0x100
	s_addc_u32 s13, s13, 0
	s_add_u32 s52, s52, 0x100
	s_addc_u32 s53, s53, 0
	s_cmp_gt_u32 s80, 61
	s_cbranch_scc0 .LBB0_153
	s_and_b64 vcc, exec, s[34:35]
	s_cbranch_vccnz .LBB0_164
	s_ashr_i32 s39, s1, 2
	s_cmp_lt_i32 s39, 13
	s_mov_b64 s[12:13], -1
	s_cbranch_scc1 .LBB0_165

;     template <int ACT, int AUX> __device__ __forceinline__ void run(const f32x4 (&acc)[2][2][4][2], const Unit& uu, int wr, int wc, int fr, int fq) const {
;     ...
;         const int row0 = u.pm * BM + wr * 64 + fr, col0 = u.pn * BM + wc * 32 + 8 * fq;
;         float rsv[8];
; #pragma unroll
;         for (int i = 0; i < 8; ++i) rsv[i] = ss[row0 + (i >> 2) * HALF + (i & 3) * 16];
;         asm volatile("" ::: "memory");
; #pragma unroll
;         for (int i = 0; i < 8; ++i) rsv[i] = __builtin_amdgcn_rsqf(rsv[i] * (1.0f / cfg::DM) + cfg::RMS_EPS);
;         float cs[2][8]; float mx[2][2];
;         if (AUX == 1) {
; #pragma unroll
;             for (int i = 0; i < 16; ++i) cs[i >> 3][i & 7] = 0.f; }
;         if (AUX == 2) { mx[0][0] = mx[0][1] = mx[1][0] = mx[1][1] = 0.f; }
; #pragma unroll
;         for (int ai = 0; ai < 2; ++ai)
; #pragma unroll
;             for (int m = 0; m < 4; ++m) { const int r = row0 + ai * HALF + m * 16; const float rs = rsv[ai * 4 + m];
;                 bf16_t* rowp = O + (size_t)r * cfg::NC + col0; float s1 = 0.f, s2 = 0.f;
; #pragma unroll
;                 for (int bj = 0; bj < 2; ++bj) { f32x4 v0 = acc[ai][bj][m][0] * rs, v1 = acc[ai][bj][m][1] * rs;
; #pragma unroll
;                     for (int j = 0; j < 4; ++j) { v0[j] = act_f<ACT>(v0[j]); v1[j] = act_f<ACT>(v1[j]); }
;                     if (AUX == 4) {
;                         unsigned q[8];
; #pragma unroll
;                         for (int j = 0; j < 4; ++j) { q[j] = (unsigned)fminf(fmaxf(fmaf(v0[j], 255.0f, 0.5f), 1.0f), 255.0f); q[4 + j] = (unsigned)fminf(fmaxf(fmaf(v1[j], 255.0f, 0.5f), 1.0f), 255.0f); }
;                         u32x2 w8; w8.x = q[0] | (q[1] << 8) | (q[2] << 16) | (q[3] << 24); w8.y = q[4] | (q[5] << 8) | (q[6] << 16) | (q[7] << 24);
;                         __builtin_nontemporal_store(w8, (u32x2*)(g8 + ((size_t)((u.pn - 52) >> 4) * cfg::MT + r) * cfg::DM + ((u.pn - 52) & 15) * BM + wc * 32 + 8 * fq + bj * HALF));
;                     } else {
;                     u32x4 w; w.x = cvt_pk_bf16(v0[0], v0[1]); w.y = cvt_pk_bf16(v0[2], v0[3]); w.z = cvt_pk_bf16(v1[0], v1[1]); w.w = cvt_pk_bf16(v1[2], v1[3]);
;                     __builtin_nontemporal_store(w, (u32x4*)(rowp + bj * HALF)); }
.LBB0_207:
	s_and_b64 vcc, exec, s[48:49]
	s_cbranch_vccz .LBB0_209
	v_lshl_add_u32 v146, s2, 8, v1
	s_waitcnt lgkmcnt(0)
	v_ashrrev_i32_e32 v147, 31, v146
	v_lshl_add_u64 v[148:149], v[146:147], 2, s[22:23]
	global_load_dword v150, v[148:149], off
	global_load_dword v152, v[148:149], off offset:64
	global_load_dword v154, v[148:149], off offset:128
	global_load_dword v156, v[148:149], off offset:192
	global_load_dword v166, v[148:149], off offset:512
	global_load_dword v168, v[148:149], off offset:576
	global_load_dword v170, v[148:149], off offset:640
	global_load_dword v172, v[148:149], off offset:704
	v_and_b32_e32 v158, 0xfffffff7, v146
	v_and_b32_e32 v159, 0x60, v191
	v_and_b32_e32 v160, 24, v191
	v_and_b32_e32 v161, 8, v146
	v_lshlrev_b32_e32 v159, 1, v159
	v_lshlrev_b32_e32 v161, 2, v161
	v_or3_b32 v159, v159, v160, v161
	v_lshl_or_b32 v159, s1, 8, v159
	v_lshlrev_b32_e32 v160, 1, v159
	v_mov_b32_e32 v161, 0
	s_mov_b32 s39, 0xe800
	v_mov_b64_e32 v[162:163], s[20:21]
	v_mad_i64_i32 v[162:163], s[12:13], v158, s39, v[162:163]
	v_lshl_add_u64 v[162:163], v[162:163], 0, v[160:161]
	s_mov_b32 s100, 0x74000
	s_mov_b32 s101, 0
	s_mov_b64 s[50:51], 0
	s_waitcnt vmcnt(0)
	v_fmamk_f32 v150, v150, 0x39800000, v221
	v_fmamk_f32 v152, v152, 0x39800000, v221
	v_fmamk_f32 v154, v154, 0x39800000, v221
	v_fmamk_f32 v156, v156, 0x39800000, v221
	v_fmamk_f32 v166, v166, 0x39800000, v221
	v_fmamk_f32 v168, v168, 0x39800000, v221
	v_fmamk_f32 v170, v170, 0x39800000, v221
	v_fmamk_f32 v172, v172, 0x39800000, v221
	v_rsq_f32_e32 v150, v150
	v_rsq_f32_e32 v152, v152
	v_rsq_f32_e32 v154, v154
	v_rsq_f32_e32 v156, v156
	v_rsq_f32_e32 v166, v166
	v_rsq_f32_e32 v168, v168
	v_rsq_f32_e32 v170, v170
	v_rsq_f32_e32 v172, v172
	v_pk_mul_f32 v[128:129], v[128:129], v[150:151] op_sel_hi:[1,0]
	v_pk_mul_f32 v[130:131], v[130:131], v[150:151] op_sel_hi:[1,0]
	v_pk_mul_f32 v[124:125], v[124:125], v[150:151] op_sel_hi:[1,0]
	v_pk_mul_f32 v[126:127], v[126:127], v[150:151] op_sel_hi:[1,0]
	v_pk_mul_f32 v[120:121], v[120:121], v[150:151] op_sel_hi:[1,0]
	v_pk_mul_f32 v[122:123], v[122:123], v[150:151] op_sel_hi:[1,0]
	v_pk_mul_f32 v[116:117], v[116:117], v[150:151] op_sel_hi:[1,0]
	v_pk_mul_f32 v[118:119], v[118:119], v[150:151] op_sel_hi:[1,0]
	v_cvt_pk_bf16_f32 v128, v128, v129
	v_cvt_pk_bf16_f32 v129, v130, v131
	v_cvt_pk_bf16_f32 v130, v124, v125
	v_cvt_pk_bf16_f32 v131, v126, v127
	v_cvt_pk_bf16_f32 v120, v120, v121
	v_cvt_pk_bf16_f32 v121, v122, v123
	v_cvt_pk_bf16_f32 v122, v116, v117
	v_cvt_pk_bf16_f32 v123, v118, v119
	v_mov_b32_e32 v124, v120
	v_mov_b32_e32 v125, v121
	v_mov_b32_e32 v126, v122
	v_mov_b32_e32 v127, v123
	v_mov_b32_dpp v120, v128 row_shl:8 row_mask:0xf bank_mask:0x3
	v_mov_b32_dpp v121, v129 row_shl:8 row_mask:0xf bank_mask:0x3
	v_mov_b32_dpp v122, v130 row_shl:8 row_mask:0xf bank_mask:0x3
	v_mov_b32_dpp v123, v131 row_shl:8 row_mask:0xf bank_mask:0x3
	v_mov_b32_dpp v128, v124 row_shr:8 row_mask:0xf bank_mask:0xc
	v_mov_b32_dpp v129, v125 row_shr:8 row_mask:0xf bank_mask:0xc
	v_mov_b32_dpp v130, v126 row_shr:8 row_mask:0xf bank_mask:0xc
	v_mov_b32_dpp v131, v127 row_shr:8 row_mask:0xf bank_mask:0xc
	v_lshl_add_u64 v[164:165], v[162:163], 0, s[100:101]
	global_store_dwordx4 v[162:163], v[128:131], off nt
	global_store_dwordx4 v[164:165], v[120:123], off nt
	v_lshl_add_u64 v[162:163], v[164:165], 0, s[100:101]
	v_pk_mul_f32 v[112:113], v[112:113], v[152:153] op_sel_hi:[1,0]
	v_pk_mul_f32 v[114:115], v[114:115], v[152:153] op_sel_hi:[1,0]
	v_pk_mul_f32 v[108:109], v[108:109], v[152:153] op_sel_hi:[1,0]
	v_pk_mul_f32 v[110:111], v[110:111], v[152:153] op_sel_hi:[1,0]
	v_pk_mul_f32 v[104:105], v[104:105], v[152:153] op_sel_hi:[1,0]
	v_pk_mul_f32 v[106:107], v[106:107], v[152:153] op_sel_hi:[1,0]
	v_pk_mul_f32 v[100:101], v[100:101], v[152:153] op_sel_hi:[1,0]
	v_pk_mul_f32 v[102:103], v[102:103], v[152:153] op_sel_hi:[1,0]
	v_cvt_pk_bf16_f32 v112, v112, v113
	v_cvt_pk_bf16_f32 v113, v114, v115
	v_cvt_pk_bf16_f32 v114, v108, v109
	v_cvt_pk_bf16_f32 v115, v110, v111
	v_cvt_pk_bf16_f32 v104, v104, v105
	v_cvt_pk_bf16_f32 v105, v106, v107
	v_cvt_pk_bf16_f32 v106, v100, v101
	v_cvt_pk_bf16_f32 v107, v102, v103
	v_mov_b32_e32 v108, v104
	v_mov_b32_e32 v109, v105
	v_mov_b32_e32 v110, v106
	v_mov_b32_e32 v111, v107
	v_mov_b32_dpp v104, v112 row_shl:8 row_mask:0xf bank_mask:0x3
	v_mov_b32_dpp v105, v113 row_shl:8 row_mask:0xf bank_mask:0x3
	v_mov_b32_dpp v106, v114 row_shl:8 row_mask:0xf bank_mask:0x3
	v_mov_b32_dpp v107, v115 row_shl:8 row_mask:0xf bank_mask:0x3
	v_mov_b32_dpp v112, v108 row_shr:8 row_mask:0xf bank_mask:0xc
	v_mov_b32_dpp v113, v109 row_shr:8 row_mask:0xf bank_mask:0xc
	v_mov_b32_dpp v114, v110 row_shr:8 row_mask:0xf bank_mask:0xc
	v_mov_b32_dpp v115, v111 row_shr:8 row_mask:0xf bank_mask:0xc
	v_lshl_add_u64 v[164:165], v[162:163], 0, s[100:101]
	global_store_dwordx4 v[162:163], v[112:115], off nt
	global_store_dwordx4 v[164:165], v[104:107], off nt
	v_lshl_add_u64 v[162:163], v[164:165], 0, s[100:101]
	v_pk_mul_f32 v[96:97], v[96:97], v[154:155] op_sel_hi:[1,0]
	v_pk_mul_f32 v[98:99], v[98:99], v[154:155] op_sel_hi:[1,0]
	v_pk_mul_f32 v[92:93], v[92:93], v[154:155] op_sel_hi:[1,0]
	v_pk_mul_f32 v[94:95], v[94:95], v[154:155] op_sel_hi:[1,0]
	v_pk_mul_f32 v[88:89], v[88:89], v[154:155] op_sel_hi:[1,0]
	v_pk_mul_f32 v[90:91], v[90:91], v[154:155] op_sel_hi:[1,0]
	v_pk_mul_f32 v[84:85], v[84:85], v[154:155] op_sel_hi:[1,0]
	v_pk_mul_f32 v[86:87], v[86:87], v[154:155] op_sel_hi:[1,0]
	v_cvt_pk_bf16_f32 v96, v96, v97
	v_cvt_pk_bf16_f32 v97, v98, v99
	v_cvt_pk_bf16_f32 v98, v92, v93
	v_cvt_pk_bf16_f32 v99, v94, v95
	v_cvt_pk_bf16_f32 v88, v88, v89
; __device__ __forceinline__ unsigned cvt_pk_bf16(float lo, float hi) { f32x2_t v = {lo, hi}; bf16x2_t b = __builtin_convertvector(v, bf16x2_t); return __builtin_bit_cast(unsigned, b); }
;     template <int ACT, int AUX> __device__ __forceinline__ void run(const f32x4 (&acc)[2][2][4][2], const Unit& uu, int wr, int wc, int fr, int fq) const {
;     ...
;             for (int m = 0; m < 4; ++m) { const int r = row0 + ai * HALF + m * 16; const float rs = rsv[ai * 4 + m];
;                 bf16_t* rowp = O + (size_t)r * cfg::NC + col0; float s1 = 0.f, s2 = 0.f;
; #pragma unroll
;                 for (int bj = 0; bj < 2; ++bj) { f32x4 v0 = acc[ai][bj][m][0] * rs, v1 = acc[ai][bj][m][1] * rs;
; #pragma unroll
;                     for (int j = 0; j < 4; ++j) { v0[j] = act_f<ACT>(v0[j]); v1[j] = act_f<ACT>(v1[j]); }
;                     if (AUX == 4) {
;                         unsigned q[8];
; #pragma unroll
;                         for (int j = 0; j < 4; ++j) { q[j] = (unsigned)fminf(fmaxf(fmaf(v0[j], 255.0f, 0.5f), 1.0f), 255.0f); q[4 + j] = (unsigned)fminf(fmaxf(fmaf(v1[j], 255.0f, 0.5f), 1.0f), 255.0f); }
;                         u32x2 w8; w8.x = q[0] | (q[1] << 8) | (q[2] << 16) | (q[3] << 24); w8.y = q[4] | (q[5] << 8) | (q[6] << 16) | (q[7] << 24);
;                         __builtin_nontemporal_store(w8, (u32x2*)(g8 + ((size_t)((u.pn - 52) >> 4) * cfg::MT + r) * cfg::DM + ((u.pn - 52) & 15) * BM + wc * 32 + 8 * fq + bj * HALF));
;                     } else {
;                     u32x4 w; w.x = cvt_pk_bf16(v0[0], v0[1]); w.y = cvt_pk_bf16(v0[2], v0[3]); w.z = cvt_pk_bf16(v1[0], v1[1]); w.w = cvt_pk_bf16(v1[2], v1[3]);
;                     __builtin_nontemporal_store(w, (u32x4*)(rowp + bj * HALF)); }
	v_cvt_pk_bf16_f32 v89, v90, v91
	v_cvt_pk_bf16_f32 v90, v84, v85
	v_cvt_pk_bf16_f32 v91, v86, v87
	v_mov_b32_e32 v92, v88
	v_mov_b32_e32 v93, v89
	v_mov_b32_e32 v94, v90
	v_mov_b32_e32 v95, v91
	v_mov_b32_dpp v88, v96 row_shl:8 row_mask:0xf bank_mask:0x3
	v_mov_b32_dpp v89, v97 row_shl:8 row_mask:0xf bank_mask:0x3
	v_mov_b32_dpp v90, v98 row_shl:8 row_mask:0xf bank_mask:0x3
	v_mov_b32_dpp v91, v99 row_shl:8 row_mask:0xf bank_mask:0x3
	v_mov_b32_dpp v96, v92 row_shr:8 row_mask:0xf bank_mask:0xc
	v_mov_b32_dpp v97, v93 row_shr:8 row_mask:0xf bank_mask:0xc
	v_mov_b32_dpp v98, v94 row_shr:8 row_mask:0xf bank_mask:0xc
	v_mov_b32_dpp v99, v95 row_shr:8 row_mask:0xf bank_mask:0xc
	v_lshl_add_u64 v[164:165], v[162:163], 0, s[100:101]
	global_store_dwordx4 v[162:163], v[96:99], off nt
	global_store_dwordx4 v[164:165], v[88:91], off nt
	v_lshl_add_u64 v[162:163], v[164:165], 0, s[100:101]
	v_pk_mul_f32 v[80:81], v[80:81], v[156:157] op_sel_hi:[1,0]
	v_pk_mul_f32 v[82:83], v[82:83], v[156:157] op_sel_hi:[1,0]
	v_pk_mul_f32 v[76:77], v[76:77], v[156:157] op_sel_hi:[1,0]
	v_pk_mul_f32 v[78:79], v[78:79], v[156:157] op_sel_hi:[1,0]
	v_pk_mul_f32 v[72:73], v[72:73], v[156:157] op_sel_hi:[1,0]
	v_pk_mul_f32 v[74:75], v[74:75], v[156:157] op_sel_hi:[1,0]
	v_pk_mul_f32 v[68:69], v[68:69], v[156:157] op_sel_hi:[1,0]
	v_pk_mul_f32 v[70:71], v[70:71], v[156:157] op_sel_hi:[1,0]
	v_cvt_pk_bf16_f32 v80, v80, v81
	v_cvt_pk_bf16_f32 v81, v82, v83
	v_cvt_pk_bf16_f32 v82, v76, v77
	v_cvt_pk_bf16_f32 v83, v78, v79
	v_cvt_pk_bf16_f32 v72, v72, v73
	v_cvt_pk_bf16_f32 v73, v74, v75
	v_cvt_pk_bf16_f32 v74, v68, v69
	v_cvt_pk_bf16_f32 v75, v70, v71
	v_mov_b32_e32 v76, v72
	v_mov_b32_e32 v77, v73
	v_mov_b32_e32 v78, v74
	v_mov_b32_e32 v79, v75
	v_mov_b32_dpp v72, v80 row_shl:8 row_mask:0xf bank_mask:0x3
	v_mov_b32_dpp v73, v81 row_shl:8 row_mask:0xf bank_mask:0x3
	v_mov_b32_dpp v74, v82 row_shl:8 row_mask:0xf bank_mask:0x3
	v_mov_b32_dpp v75, v83 row_shl:8 row_mask:0xf bank_mask:0x3
	v_mov_b32_dpp v80, v76 row_shr:8 row_mask:0xf bank_mask:0xc
	v_mov_b32_dpp v81, v77 row_shr:8 row_mask:0xf bank_mask:0xc
	v_mov_b32_dpp v82, v78 row_shr:8 row_mask:0xf bank_mask:0xc
	v_mov_b32_dpp v83, v79 row_shr:8 row_mask:0xf bank_mask:0xc
	v_lshl_add_u64 v[164:165], v[162:163], 0, s[100:101]
	global_store_dwordx4 v[162:163], v[80:83], off nt
	global_store_dwordx4 v[164:165], v[72:75], off nt
	s_mov_b32 s100, 0x488000
	v_lshl_add_u64 v[162:163], v[162:163], 0, s[100:101]
	s_mov_b32 s100, 0x74000
	v_pk_mul_f32 v[64:65], v[64:65], v[166:167] op_sel_hi:[1,0]
	v_pk_mul_f32 v[66:67], v[66:67], v[166:167] op_sel_hi:[1,0]
	v_pk_mul_f32 v[60:61], v[60:61], v[166:167] op_sel_hi:[1,0]
	v_pk_mul_f32 v[62:63], v[62:63], v[166:167] op_sel_hi:[1,0]
	v_pk_mul_f32 v[56:57], v[56:57], v[166:167] op_sel_hi:[1,0]
	v_pk_mul_f32 v[58:59], v[58:59], v[166:167] op_sel_hi:[1,0]
	v_pk_mul_f32 v[52:53], v[52:53], v[166:167] op_sel_hi:[1,0]
	v_pk_mul_f32 v[54:55], v[54:55], v[166:167] op_sel_hi:[1,0]
	v_cvt_pk_bf16_f32 v64, v64, v65
	v_cvt_pk_bf16_f32 v65, v66, v67
	v_cvt_pk_bf16_f32 v66, v60, v61
	v_cvt_pk_bf16_f32 v67, v62, v63
	v_cvt_pk_bf16_f32 v56, v56, v57
	v_cvt_pk_bf16_f32 v57, v58, v59
	v_cvt_pk_bf16_f32 v58, v52, v53
	v_cvt_pk_bf16_f32 v59, v54, v55
	v_mov_b32_e32 v60, v56
	v_mov_b32_e32 v61, v57
	v_mov_b32_e32 v62, v58
	v_mov_b32_e32 v63, v59
	v_mov_b32_dpp v56, v64 row_shl:8 row_mask:0xf bank_mask:0x3
	v_mov_b32_dpp v57, v65 row_shl:8 row_mask:0xf bank_mask:0x3
	v_mov_b32_dpp v58, v66 row_shl:8 row_mask:0xf bank_mask:0x3
	v_mov_b32_dpp v59, v67 row_shl:8 row_mask:0xf bank_mask:0x3
	v_mov_b32_dpp v64, v60 row_shr:8 row_mask:0xf bank_mask:0xc
	v_mov_b32_dpp v65, v61 row_shr:8 row_mask:0xf bank_mask:0xc
	v_mov_b32_dpp v66, v62 row_shr:8 row_mask:0xf bank_mask:0xc
	v_mov_b32_dpp v67, v63 row_shr:8 row_mask:0xf bank_mask:0xc
	v_lshl_add_u64 v[164:165], v[162:163], 0, s[100:101]
	global_store_dwordx4 v[162:163], v[64:67], off nt
	global_store_dwordx4 v[164:165], v[56:59], off nt
	v_lshl_add_u64 v[162:163], v[164:165], 0, s[100:101]
	v_pk_mul_f32 v[48:49], v[48:49], v[168:169] op_sel_hi:[1,0]
	v_pk_mul_f32 v[50:51], v[50:51], v[168:169] op_sel_hi:[1,0]
	v_pk_mul_f32 v[44:45], v[44:45], v[168:169] op_sel_hi:[1,0]
	v_pk_mul_f32 v[46:47], v[46:47], v[168:169] op_sel_hi:[1,0]
; __device__ __forceinline__ unsigned cvt_pk_bf16(float lo, float hi) { f32x2_t v = {lo, hi}; bf16x2_t b = __builtin_convertvector(v, bf16x2_t); return __builtin_bit_cast(unsigned, b); }
;     template <int ACT, int AUX> __device__ __forceinline__ void run(const f32x4 (&acc)[2][2][4][2], const Unit& uu, int wr, int wc, int fr, int fq) const {
;     ...
;             for (int m = 0; m < 4; ++m) { const int r = row0 + ai * HALF + m * 16; const float rs = rsv[ai * 4 + m];
;                 bf16_t* rowp = O + (size_t)r * cfg::NC + col0; float s1 = 0.f, s2 = 0.f;
; #pragma unroll
;                 for (int bj = 0; bj < 2; ++bj) { f32x4 v0 = acc[ai][bj][m][0] * rs, v1 = acc[ai][bj][m][1] * rs;
; #pragma unroll
;                     for (int j = 0; j < 4; ++j) { v0[j] = act_f<ACT>(v0[j]); v1[j] = act_f<ACT>(v1[j]); }
;                     if (AUX == 4) {
;                         unsigned q[8];
; #pragma unroll
;                         for (int j = 0; j < 4; ++j) { q[j] = (unsigned)fminf(fmaxf(fmaf(v0[j], 255.0f, 0.5f), 1.0f), 255.0f); q[4 + j] = (unsigned)fminf(fmaxf(fmaf(v1[j], 255.0f, 0.5f), 1.0f), 255.0f); }
;                         u32x2 w8; w8.x = q[0] | (q[1] << 8) | (q[2] << 16) | (q[3] << 24); w8.y = q[4] | (q[5] << 8) | (q[6] << 16) | (q[7] << 24);
;                         __builtin_nontemporal_store(w8, (u32x2*)(g8 + ((size_t)((u.pn - 52) >> 4) * cfg::MT + r) * cfg::DM + ((u.pn - 52) & 15) * BM + wc * 32 + 8 * fq + bj * HALF));
;                     } else {
;                     u32x4 w; w.x = cvt_pk_bf16(v0[0], v0[1]); w.y = cvt_pk_bf16(v0[2], v0[3]); w.z = cvt_pk_bf16(v1[0], v1[1]); w.w = cvt_pk_bf16(v1[2], v1[3]);
;                     __builtin_nontemporal_store(w, (u32x4*)(rowp + bj * HALF)); }
	v_pk_mul_f32 v[40:41], v[40:41], v[168:169] op_sel_hi:[1,0]
	v_pk_mul_f32 v[42:43], v[42:43], v[168:169] op_sel_hi:[1,0]
	v_pk_mul_f32 v[36:37], v[36:37], v[168:169] op_sel_hi:[1,0]
	v_pk_mul_f32 v[38:39], v[38:39], v[168:169] op_sel_hi:[1,0]
	v_cvt_pk_bf16_f32 v48, v48, v49
	v_cvt_pk_bf16_f32 v49, v50, v51
	v_cvt_pk_bf16_f32 v50, v44, v45
	v_cvt_pk_bf16_f32 v51, v46, v47
	v_cvt_pk_bf16_f32 v40, v40, v41
	v_cvt_pk_bf16_f32 v41, v42, v43
	v_cvt_pk_bf16_f32 v42, v36, v37
	v_cvt_pk_bf16_f32 v43, v38, v39
	v_mov_b32_e32 v44, v40
	v_mov_b32_e32 v45, v41
	v_mov_b32_e32 v46, v42
	v_mov_b32_e32 v47, v43
	v_mov_b32_dpp v40, v48 row_shl:8 row_mask:0xf bank_mask:0x3
	v_mov_b32_dpp v41, v49 row_shl:8 row_mask:0xf bank_mask:0x3
	v_mov_b32_dpp v42, v50 row_shl:8 row_mask:0xf bank_mask:0x3
	v_mov_b32_dpp v43, v51 row_shl:8 row_mask:0xf bank_mask:0x3
	v_mov_b32_dpp v48, v44 row_shr:8 row_mask:0xf bank_mask:0xc
	v_mov_b32_dpp v49, v45 row_shr:8 row_mask:0xf bank_mask:0xc
	v_mov_b32_dpp v50, v46 row_shr:8 row_mask:0xf bank_mask:0xc
	v_mov_b32_dpp v51, v47 row_shr:8 row_mask:0xf bank_mask:0xc
	v_lshl_add_u64 v[164:165], v[162:163], 0, s[100:101]
	global_store_dwordx4 v[162:163], v[48:51], off nt
	global_store_dwordx4 v[164:165], v[40:43], off nt
	v_lshl_add_u64 v[162:163], v[164:165], 0, s[100:101]
	v_pk_mul_f32 v[32:33], v[32:33], v[170:171] op_sel_hi:[1,0]
	v_pk_mul_f32 v[34:35], v[34:35], v[170:171] op_sel_hi:[1,0]
	v_pk_mul_f32 v[28:29], v[28:29], v[170:171] op_sel_hi:[1,0]
	v_pk_mul_f32 v[30:31], v[30:31], v[170:171] op_sel_hi:[1,0]
	v_pk_mul_f32 v[24:25], v[24:25], v[170:171] op_sel_hi:[1,0]
	v_pk_mul_f32 v[26:27], v[26:27], v[170:171] op_sel_hi:[1,0]
	v_pk_mul_f32 v[20:21], v[20:21], v[170:171] op_sel_hi:[1,0]
	v_pk_mul_f32 v[22:23], v[22:23], v[170:171] op_sel_hi:[1,0]
	v_cvt_pk_bf16_f32 v32, v32, v33
	v_cvt_pk_bf16_f32 v33, v34, v35
	v_cvt_pk_bf16_f32 v34, v28, v29
	v_cvt_pk_bf16_f32 v35, v30, v31
	v_cvt_pk_bf16_f32 v24, v24, v25
	v_cvt_pk_bf16_f32 v25, v26, v27
	v_cvt_pk_bf16_f32 v26, v20, v21
	v_cvt_pk_bf16_f32 v27, v22, v23
	v_mov_b32_e32 v28, v24
	v_mov_b32_e32 v29, v25
	v_mov_b32_e32 v30, v26
	v_mov_b32_e32 v31, v27
	v_mov_b32_dpp v24, v32 row_shl:8 row_mask:0xf bank_mask:0x3
	v_mov_b32_dpp v25, v33 row_shl:8 row_mask:0xf bank_mask:0x3
	v_mov_b32_dpp v26, v34 row_shl:8 row_mask:0xf bank_mask:0x3
	v_mov_b32_dpp v27, v35 row_shl:8 row_mask:0xf bank_mask:0x3
	v_mov_b32_dpp v32, v28 row_shr:8 row_mask:0xf bank_mask:0xc
	v_mov_b32_dpp v33, v29 row_shr:8 row_mask:0xf bank_mask:0xc
	v_mov_b32_dpp v34, v30 row_shr:8 row_mask:0xf bank_mask:0xc
	v_mov_b32_dpp v35, v31 row_shr:8 row_mask:0xf bank_mask:0xc
	v_lshl_add_u64 v[164:165], v[162:163], 0, s[100:101]
	global_store_dwordx4 v[162:163], v[32:35], off nt
	global_store_dwordx4 v[164:165], v[24:27], off nt
	v_lshl_add_u64 v[162:163], v[164:165], 0, s[100:101]
	v_pk_mul_f32 v[16:17], v[16:17], v[172:173] op_sel_hi:[1,0]
	v_pk_mul_f32 v[18:19], v[18:19], v[172:173] op_sel_hi:[1,0]
	v_pk_mul_f32 v[12:13], v[12:13], v[172:173] op_sel_hi:[1,0]
	v_pk_mul_f32 v[14:15], v[14:15], v[172:173] op_sel_hi:[1,0]
	v_pk_mul_f32 v[8:9], v[8:9], v[172:173] op_sel_hi:[1,0]
	v_pk_mul_f32 v[10:11], v[10:11], v[172:173] op_sel_hi:[1,0]
	v_pk_mul_f32 v[4:5], v[4:5], v[172:173] op_sel_hi:[1,0]
	v_pk_mul_f32 v[6:7], v[6:7], v[172:173] op_sel_hi:[1,0]
	v_cvt_pk_bf16_f32 v16, v16, v17
	v_cvt_pk_bf16_f32 v17, v18, v19
	v_cvt_pk_bf16_f32 v18, v12, v13
	v_cvt_pk_bf16_f32 v19, v14, v15
	v_cvt_pk_bf16_f32 v8, v8, v9
	v_cvt_pk_bf16_f32 v9, v10, v11
	v_cvt_pk_bf16_f32 v10, v4, v5
	v_cvt_pk_bf16_f32 v11, v6, v7
	v_mov_b32_e32 v12, v8
	v_mov_b32_e32 v13, v9
	v_mov_b32_e32 v14, v10
	v_mov_b32_e32 v15, v11
	v_mov_b32_dpp v8, v16 row_shl:8 row_mask:0xf bank_mask:0x3
	v_mov_b32_dpp v9, v17 row_shl:8 row_mask:0xf bank_mask:0x3
	v_mov_b32_dpp v10, v18 row_shl:8 row_mask:0xf bank_mask:0x3
	v_mov_b32_dpp v11, v19 row_shl:8 row_mask:0xf bank_mask:0x3
	v_mov_b32_dpp v16, v12 row_shr:8 row_mask:0xf bank_mask:0xc
	v_mov_b32_dpp v17, v13 row_shr:8 row_mask:0xf bank_mask:0xc
	v_mov_b32_dpp v18, v14 row_shr:8 row_mask:0xf bank_mask:0xc
	v_mov_b32_dpp v19, v15 row_shr:8 row_mask:0xf bank_mask:0xc
	v_lshl_add_u64 v[164:165], v[162:163], 0, s[100:101]
	global_store_dwordx4 v[162:163], v[16:19], off nt
	global_store_dwordx4 v[164:165], v[8:11], off nt
